# MLA fast path barrier-locked ping-pong: waves 4-7 one phase behind waves 0-3, 5 phases per interval
# baseline (speedup 1.0000x reference)
.Linit_done:
	s_waitcnt lgkmcnt(0)
	s_barrier
	v_mfma_f32_32x32x16_bf16 v[16:31], v[90:93], v[144:147], v[16:31]
	v_lshlrev_b32_e32 v145, 2, v204
	s_waitcnt vmcnt(5)
	v_pk_mul_f32 v[48:49], v[48:49], v[56:57] op_sel:[0,1] op_sel_hi:[0,0]
	v_pk_fma_f32 v[50:51], v[44:45], v[56:57], v[48:49] neg_lo:[0,0,1] neg_hi:[0,0,1]
	v_pk_fma_f32 v[44:45], v[44:45], v[56:57], v[48:49] op_sel_hi:[0,1,1]
	v_mul_f32_e32 v44, v168, v46
	v_mul_f32_e32 v46, v168, v47
	v_pk_mul_f32 v[46:47], v[46:47], v[58:59] op_sel:[0,1] op_sel_hi:[0,0]
	v_mfma_f32_32x32x16_bf16 v[16:31], v[82:85], v[140:143], v[16:31]
	v_fma_f32 v48, v44, v58, -v46
	v_fma_f32 v49, v45, v59, -v47
	v_fma_f32 v46, v44, v58, v46
	v_fma_f32 v47, v44, v59, v47
	v_mul_f32_e32 v44, v168, v41
	s_waitcnt vmcnt(4)
	v_pk_mul_f32 v[52:53], v[44:45], v[60:61] op_sel:[0,1] op_sel_hi:[0,0]
	v_pk_fma_f32 v[54:55], v[40:41], v[60:61], v[52:53] neg_lo:[0,0,1] neg_hi:[0,0,1]
	v_pk_fma_f32 v[40:41], v[40:41], v[60:61], v[52:53] op_sel_hi:[0,1,1]
	v_mul_f32_e32 v40, v168, v42
	v_mfma_f32_32x32x16_bf16 v[16:31], v[160:163], v[132:135], v[16:31]
	v_mul_f32_e32 v42, v168, v43
	v_pk_mul_f32 v[42:43], v[42:43], v[62:63] op_sel:[0,1] op_sel_hi:[0,0]
	v_pk_fma_f32 v[52:53], v[40:41], v[62:63], v[42:43] neg_lo:[0,0,1] neg_hi:[0,0,1]
	v_pk_fma_f32 v[42:43], v[40:41], v[62:63], v[42:43] op_sel_hi:[0,1,1]
	v_cvt_pk_bf16_f32 v132, v54, v41
	v_cvt_pk_bf16_f32 v133, v52, v43
	v_cvt_pk_bf16_f32 v134, v50, v45
	v_mfma_f32_32x32x16_bf16 v[16:31], v[176:179], v[136:139], v[16:31]
	v_cvt_pk_bf16_f32 v135, v48, v47
	v_mov_b64_e32 v[62:63], v[14:15]
	v_mov_b64_e32 v[60:61], v[12:13]
	v_mov_b64_e32 v[58:59], v[10:11]
	v_mov_b64_e32 v[56:57], v[8:9]
	v_mov_b64_e32 v[54:55], v[6:7]
	v_mov_b64_e32 v[52:53], v[4:5]
	s_nop 4
	v_mul_f32_e32 v40, v168, v21
	v_mul_f32_e32 v20, v168, v20
	s_waitcnt vmcnt(2)
	v_pk_mul_f32 v[40:41], v[40:41], v[64:65] op_sel:[0,1] op_sel_hi:[0,0]
	v_pk_fma_f32 v[42:43], v[20:21], v[64:65], v[40:41] neg_lo:[0,0,1] neg_hi:[0,0,1]
	v_pk_fma_f32 v[20:21], v[20:21], v[64:65], v[40:41] op_sel_hi:[0,1,1]
	v_mul_f32_e32 v20, v168, v22
	v_mul_f32_e32 v22, v168, v23
	v_pk_mul_f32 v[22:23], v[22:23], v[66:67] op_sel:[0,1] op_sel_hi:[0,0]
	v_pk_fma_f32 v[40:41], v[20:21], v[66:67], v[22:23] neg_lo:[0,0,1] neg_hi:[0,0,1]
	v_pk_fma_f32 v[22:23], v[20:21], v[66:67], v[22:23] op_sel_hi:[0,1,1]
	v_mul_f32_e32 v20, v168, v17
	v_mul_f32_e32 v16, v168, v16
	v_pk_mul_f32 v[44:45], v[20:21], v[164:165] op_sel:[0,1] op_sel_hi:[0,0]
	v_pk_fma_f32 v[46:47], v[16:17], v[164:165], v[44:45] neg_lo:[0,0,1] neg_hi:[0,0,1]
	v_pk_fma_f32 v[16:17], v[16:17], v[164:165], v[44:45] op_sel_hi:[0,1,1]
	v_mul_f32_e32 v16, v168, v18
	v_mul_f32_e32 v18, v168, v19
	v_pk_mul_f32 v[18:19], v[18:19], v[166:167] op_sel:[0,1] op_sel_hi:[0,0]
	v_pk_fma_f32 v[44:45], v[16:17], v[166:167], v[18:19] neg_lo:[0,0,1] neg_hi:[0,0,1]
	v_pk_fma_f32 v[18:19], v[16:17], v[166:167], v[18:19] op_sel_hi:[0,1,1]
	v_mul_f32_e32 v18, v168, v29
	v_cvt_pk_bf16_f32 v137, v44, v19
	v_mul_f32_e32 v16, v168, v28
	s_waitcnt vmcnt(1)
	v_pk_mul_f32 v[18:19], v[18:19], v[36:37] op_sel:[0,1] op_sel_hi:[0,0]
	v_cvt_pk_bf16_f32 v136, v46, v17
	v_cvt_pk_bf16_f32 v138, v42, v21
	v_pk_fma_f32 v[20:21], v[16:17], v[36:37], v[18:19] neg_lo:[0,0,1] neg_hi:[0,0,1]
	v_pk_fma_f32 v[16:17], v[16:17], v[36:37], v[18:19] op_sel_hi:[0,1,1]
	v_mul_f32_e32 v18, v168, v31
	v_mul_f32_e32 v16, v168, v30
	v_pk_mul_f32 v[18:19], v[18:19], v[38:39] op_sel:[0,1] op_sel_hi:[0,0]
	v_cvt_pk_bf16_f32 v139, v40, v23
	v_pk_fma_f32 v[22:23], v[16:17], v[38:39], v[18:19] neg_lo:[0,0,1] neg_hi:[0,0,1]
	v_pk_fma_f32 v[18:19], v[16:17], v[38:39], v[18:19] op_sel_hi:[0,1,1]
	v_mul_f32_e32 v18, v168, v25
	v_mul_f32_e32 v16, v168, v24
	s_waitcnt vmcnt(0)
	v_pk_mul_f32 v[24:25], v[18:19], v[32:33] op_sel:[0,1] op_sel_hi:[0,0]
	v_mul_f32_e32 v18, v168, v27
	v_pk_fma_f32 v[28:29], v[16:17], v[32:33], v[24:25] neg_lo:[0,0,1] neg_hi:[0,0,1]
	v_pk_fma_f32 v[24:25], v[16:17], v[32:33], v[24:25] op_sel_hi:[0,1,1]
	v_mul_f32_e32 v16, v168, v26
	v_pk_mul_f32 v[26:27], v[18:19], v[34:35] op_sel:[0,1] op_sel_hi:[0,0]
	v_pk_fma_f32 v[30:31], v[16:17], v[34:35], v[26:27] neg_lo:[0,0,1] neg_hi:[0,0,1]
	v_pk_fma_f32 v[26:27], v[16:17], v[34:35], v[26:27] op_sel_hi:[0,1,1]
	v_cvt_pk_bf16_f32 v142, v20, v17
	v_lshrrev_b32_e32 v17, 1, v203
	v_mad_u32_u24 v16, v200, s4, 0
	v_bfe_u32 v18, v203, 1, 3
	v_bitop3_b32 v17, v204, v17, 7 bitop3:0x78
	v_lshl_add_u32 v147, v17, 4, v16
	v_bitop3_b32 v17, v204, v18, 2 bitop3:0x36
	v_lshl_add_u32 v148, v17, 4, v16
	v_bitop3_b32 v17, v204, v18, 4 bitop3:0x36
	v_lshl_add_u32 v149, v17, 4, v16
	v_bitop3_b32 v17, v204, v18, 6 bitop3:0x36
	v_lshl_add_u32 v150, v17, 4, v16
	v_lshrrev_b32_e32 v16, 3, v202
	v_bfe_u32 v17, v202, 3, 1
	v_and_b32_e32 v16, 2, v16
	v_bfe_u32 v18, v203, 1, 1
	v_bfe_u32 v20, v203, 2, 1
	v_lshlrev_b32_e32 v21, 3, v17
	v_cvt_pk_bf16_f32 v143, v22, v19
	v_or_b32_e32 v19, v16, v18
	v_or3_b32 v20, v21, v20, v145
	v_lshlrev_b32_e32 v21, 1, v204
	v_bitop3_b32 v16, v16, v21, v18 bitop3:0x36
	v_bitop3_b32 v18, v21, v19, 1 bitop3:0x36
	v_cvt_f32_ubyte0_e32 v21, s25
	v_lshlrev_b32_e32 v22, 3, v203
	v_lshlrev_b32_e32 v17, 6, v17
	v_lshlrev_b32_e32 v18, 4, v18
	v_rcp_iflag_f32_e32 v21, v21
	v_and_b32_e32 v22, 8, v22
	v_mad_u32_u24 v20, v20, s4, 0
	v_or_b32_e32 v19, v18, v17
	v_lshl_add_u32 v16, v16, 4, v20
	v_add3_u32 v152, v20, v19, v22
	v_xor_b32_e32 v19, 64, v17
	v_add3_u32 v151, v16, v17, v22
	v_add3_u32 v153, v16, v19, v22
	v_bitop3_b32 v16, v18, v17, 64 bitop3:0xf6
	v_add3_u32 v154, v20, v16, v22
	v_mul_f32_e32 v16, 0x4f7ffffe, v21
	v_cvt_u32_f32_e32 v16, v16
	s_abs_i32 s4, s89
	v_cvt_pk_bf16_f32 v140, v28, v25
	v_cvt_pk_bf16_f32 v141, v30, v27
	v_readfirstlane_b32 s6, v16
	s_mul_i32 s5, s5, s6
	s_mul_hi_u32 s5, s6, s5
	s_add_i32 s6, s6, s5
	s_mul_hi_u32 s5, s4, s6
	s_mul_i32 s6, s5, s25
	s_sub_i32 s4, s4, s6
	s_add_i32 s6, s5, 1
	s_sub_i32 s7, s4, s25
	s_cmp_ge_u32 s4, s25
	s_cselect_b32 s5, s6, s5
	s_cselect_b32 s4, s7, s4
	s_add_i32 s6, s5, 1
	s_cmp_ge_u32 s4, s25
	s_cselect_b32 s4, s6, s5
	s_xor_b32 s12, s4, s11
	s_sub_i32 s8, s12, s11
	s_mul_i32 s4, s8, s25
	s_sub_i32 s4, s89, s4
	s_lshl_b32 s6, s4, 5
	s_ashr_i32 s7, s6, 31
	s_lshl_b64 s[4:5], s[6:7], 2
	s_add_u32 s4, s68, s4
	s_addc_u32 s5, s69, s5
	v_lshl_or_b32 v16, s12, 6, v196
	s_lshl_b32 s7, s11, 6
	v_subrev_u32_e32 v155, s7, v16
	s_add_i32 s7, s29, s21
	v_add_u32_e32 v16, s7, v200
	v_sub_u32_e32 v156, v16, v145
	v_mov_b64_e32 v[46:47], v[14:15]
	v_mov_b64_e32 v[30:31], v[14:15]
	s_movk_i32 s7, 0x7f
	s_mov_b32 s11, 3
	s_mov_b32 s12, s40
	v_mov_b64_e32 v[44:45], v[12:13]
	v_mov_b64_e32 v[42:43], v[10:11]
	v_mov_b64_e32 v[40:41], v[8:9]
	v_mov_b64_e32 v[38:39], v[6:7]
	v_mov_b64_e32 v[36:37], v[4:5]
	v_mov_b64_e32 v[34:35], v[2:3]
	v_mov_b64_e32 v[32:33], v[0:1]
	v_mov_b64_e32 v[50:51], v[2:3]
	v_mov_b64_e32 v[48:49], v[0:1]
	v_mov_b64_e32 v[28:29], v[12:13]
	v_mov_b64_e32 v[26:27], v[10:11]
	v_mov_b64_e32 v[24:25], v[8:9]
	v_mov_b64_e32 v[22:23], v[6:7]
	v_mov_b64_e32 v[20:21], v[4:5]
	v_mov_b64_e32 v[18:19], v[2:3]
	v_mov_b64_e32 v[16:17], v[0:1]
	s_cmp_eq_u32 s101, 0
	s_cbranch_scc1 .Lnostag_in
	s_cmp_lt_u32 s88, 0x1000
	s_cbranch_scc1 .Lnostag_in
	s_barrier
.Lnostag_in:
	s_branch .LBB0_1238
.LBB0_1237:
	v_sub_f32_e32 v64, v64, v157
	v_exp_f32_e32 v170, v64
	v_sub_f32_e32 v64, v65, v157
	v_exp_f32_e32 v171, v64
	v_sub_f32_e32 v64, v66, v157
	v_exp_f32_e32 v176, v64
	v_sub_f32_e32 v64, v67, v157
	v_exp_f32_e32 v177, v64
	v_sub_f32_e32 v64, v68, v157
	v_exp_f32_e32 v178, v64
	v_sub_f32_e32 v64, v69, v157
	v_sub_f32_e32 v80, v80, v157
	v_exp_f32_e32 v179, v64
	v_sub_f32_e32 v64, v70, v157
	v_exp_f32_e32 v161, v80
	v_sub_f32_e32 v80, v81, v157
	v_exp_f32_e32 v185, v64
	v_sub_f32_e32 v64, v71, v157
	v_exp_f32_e32 v162, v80
	v_sub_f32_e32 v80, v82, v157
	v_exp_f32_e32 v187, v64
	v_sub_f32_e32 v64, v72, v157
	v_exp_f32_e32 v163, v80
	v_sub_f32_e32 v80, v83, v157
	v_exp_f32_e32 v203, v64
	v_sub_f32_e32 v64, v73, v157
	v_exp_f32_e32 v164, v80
	v_sub_f32_e32 v80, v84, v157
	v_exp_f32_e32 v204, v64
	v_sub_f32_e32 v64, v74, v157
	v_exp_f32_e32 v165, v80
	v_sub_f32_e32 v80, v85, v157
	v_exp_f32_e32 v205, v64
	v_sub_f32_e32 v64, v75, v157
	v_exp_f32_e32 v166, v80
	v_sub_f32_e32 v80, v86, v157
	v_exp_f32_e32 v206, v64
	v_sub_f32_e32 v64, v76, v157
	v_exp_f32_e32 v167, v80
	v_sub_f32_e32 v80, v87, v157
	v_exp_f32_e32 v207, v64
	v_sub_f32_e32 v64, v77, v157
	v_add_u32_e32 v209, s14, v151
	v_exp_f32_e32 v168, v80
	v_sub_f32_e32 v80, v88, v157
	v_exp_f32_e32 v208, v64
	v_add_u32_e32 v210, s14, v152
	ds_read_b64_tr_b16 v[64:65], v209
	ds_read_b64_tr_b16 v[66:67], v210 offset:768
	v_exp_f32_e32 v88, v80
	v_sub_f32_e32 v80, v89, v157
	v_exp_f32_e32 v89, v80
	v_sub_f32_e32 v80, v90, v157
	v_exp_f32_e32 v90, v80
	v_sub_f32_e32 v80, v91, v157
	v_exp_f32_e32 v91, v80
	v_sub_f32_e32 v80, v92, v157
	v_cvt_pk_bf16_f32 v72, v161, v162
	v_cvt_pk_bf16_f32 v73, v165, v166
	v_cvt_pk_bf16_f32 v74, v163, v164
	v_cvt_pk_bf16_f32 v75, v167, v168
	v_exp_f32_e32 v92, v80
	v_sub_f32_e32 v80, v93, v157
	s_waitcnt lgkmcnt(0)
	v_mfma_f32_32x32x16_bf16 v[48:63], v[64:67], v[72:75], v[48:63]
	v_exp_f32_e32 v93, v80
	v_sub_f32_e32 v80, v94, v157
	v_exp_f32_e32 v94, v80
	v_sub_f32_e32 v80, v95, v157
	v_sub_f32_e32 v68, v78, v157
	v_exp_f32_e32 v95, v80
	v_exp_f32_e32 v211, v68
	ds_read_b64_tr_b16 v[68:69], v209 offset:6144
	ds_read_b64_tr_b16 v[70:71], v210 offset:6912
	v_sub_f32_e32 v80, v79, v157
	v_cvt_pk_bf16_f32 v76, v88, v89
	v_cvt_pk_bf16_f32 v77, v92, v93
	v_cvt_pk_bf16_f32 v78, v90, v91
	v_cvt_pk_bf16_f32 v79, v94, v95
	ds_read_b64_tr_b16 v[64:65], v209 offset:12288
	ds_read_b64_tr_b16 v[66:67], v210 offset:13056
	s_waitcnt lgkmcnt(2)
	v_mfma_f32_32x32x16_bf16 v[48:63], v[68:71], v[76:79], v[48:63]
	v_cvt_pk_bf16_f32 v68, v170, v171
	v_cvt_pk_bf16_f32 v69, v178, v179
	v_cvt_pk_bf16_f32 v70, v176, v177
	v_cvt_pk_bf16_f32 v71, v185, v187
	v_add_u32_e32 v213, s14, v153
	v_exp_f32_e32 v212, v80
	ds_read_b64_tr_b16 v[80:81], v209 offset:18432
	ds_read_b64_tr_b16 v[82:83], v210 offset:19200
	s_waitcnt lgkmcnt(2)
	v_mfma_f32_32x32x16_bf16 v[48:63], v[64:67], v[68:71], v[48:63]
	ds_read_b64_tr_b16 v[84:85], v213
	v_cvt_pk_bf16_f32 v64, v203, v204
	v_cvt_pk_bf16_f32 v65, v207, v208
	v_cvt_pk_bf16_f32 v66, v205, v206
	v_cvt_pk_bf16_f32 v67, v211, v212
	v_add_u32_e32 v214, s14, v154
	v_add_f32_e32 v159, v159, v160
	s_waitcnt lgkmcnt(1)
	v_mfma_f32_32x32x16_bf16 v[48:63], v[80:83], v[64:67], v[48:63]
	ds_read_b64_tr_b16 v[86:87], v214 offset:768
	ds_read_b64_tr_b16 v[80:81], v213 offset:6144
	v_fmac_f32_e32 v159, v158, v144
	s_addk_i32 s12, 0x1000
	s_add_i32 s11, s11, 4
	s_add_i32 s10, s10, 2
	s_addk_i32 s7, 0x80
	v_add_u32_e32 v155, 32, v155
	s_waitcnt lgkmcnt(1)
	v_mfma_f32_32x32x16_bf16 v[32:47], v[84:87], v[72:75], v[32:47]
	ds_read_b64_tr_b16 v[82:83], v214 offset:6912
	ds_read_b64_tr_b16 v[84:85], v213 offset:12288
	s_cmp_ge_u32 s13, s9
	v_add_u32_e32 v156, 0xffffff80, v156
	s_waitcnt lgkmcnt(1)
	v_mfma_f32_32x32x16_bf16 v[32:47], v[80:83], v[76:79], v[32:47]
	ds_read_b64_tr_b16 v[86:87], v214 offset:13056
	ds_read_b64_tr_b16 v[80:81], v213 offset:18432
	s_waitcnt lgkmcnt(1)
	v_mfma_f32_32x32x16_bf16 v[32:47], v[84:87], v[68:71], v[32:47]
	ds_read_b64_tr_b16 v[82:83], v214 offset:19200
	ds_read_b64_tr_b16 v[84:85], v209 offset:128
	ds_read_b64_tr_b16 v[86:87], v210 offset:896
	s_waitcnt lgkmcnt(0)
	v_mfma_f32_32x32x16_bf16 v[0:15], v[84:87], v[72:75], v[0:15]
	v_add_f32_e32 v84, 0, v161
	v_add_f32_e32 v84, v162, v84
	v_add_f32_e32 v84, v163, v84
	v_add_f32_e32 v84, v164, v84
	v_add_f32_e32 v144, v165, v84
	v_mfma_f32_32x32x16_bf16 v[32:47], v[80:83], v[64:67], v[32:47]
	ds_read_b64_tr_b16 v[80:81], v209 offset:6272
	ds_read_b64_tr_b16 v[82:83], v210 offset:7040
	ds_read_b64_tr_b16 v[84:85], v209 offset:12416
	ds_read_b64_tr_b16 v[86:87], v210 offset:13184
	s_waitcnt lgkmcnt(2)
	v_mfma_f32_32x32x16_bf16 v[0:15], v[80:83], v[76:79], v[0:15]
	v_add_f32_e32 v80, v166, v144
	v_add_f32_e32 v80, v167, v80
	v_add_f32_e32 v80, v168, v80
	v_add_f32_e32 v80, v88, v80
	v_add_f32_e32 v88, v89, v80
	ds_read_b64_tr_b16 v[80:81], v209 offset:18560
	ds_read_b64_tr_b16 v[82:83], v210 offset:19328
	s_waitcnt lgkmcnt(2)
	v_mfma_f32_32x32x16_bf16 v[0:15], v[84:87], v[68:71], v[0:15]
	v_add_f32_e32 v84, v90, v88
	v_add_f32_e32 v84, v91, v84
	v_add_f32_e32 v84, v92, v84
	v_add_f32_e32 v84, v93, v84
	v_add_f32_e32 v88, v94, v84
	ds_read_b64_tr_b16 v[84:85], v213 offset:128
	ds_read_b64_tr_b16 v[86:87], v214 offset:896
	s_waitcnt lgkmcnt(2)
	v_mfma_f32_32x32x16_bf16 v[0:15], v[80:83], v[64:67], v[0:15]
	v_add_f32_e32 v80, v95, v88
	v_add_f32_e32 v80, v170, v80
	v_add_f32_e32 v80, v171, v80
	v_add_f32_e32 v80, v176, v80
	v_add_f32_e32 v88, v177, v80
	ds_read_b64_tr_b16 v[80:81], v213 offset:6272
	ds_read_b64_tr_b16 v[82:83], v214 offset:7040
	s_waitcnt lgkmcnt(2)
	v_mfma_f32_32x32x16_bf16 v[16:31], v[84:87], v[72:75], v[16:31]
	v_add_f32_e32 v72, v178, v88
	v_add_f32_e32 v72, v179, v72
	v_add_f32_e32 v72, v185, v72
	v_add_f32_e32 v72, v187, v72
	v_add_f32_e32 v84, v203, v72
	ds_read_b64_tr_b16 v[72:73], v213 offset:12416
	ds_read_b64_tr_b16 v[74:75], v214 offset:13184
	s_waitcnt lgkmcnt(2)
	v_mfma_f32_32x32x16_bf16 v[16:31], v[80:83], v[76:79], v[16:31]
	v_add_f32_e32 v76, v204, v84
	v_add_f32_e32 v76, v205, v76
	v_add_f32_e32 v76, v206, v76
	v_add_f32_e32 v76, v207, v76
	v_add_f32_e32 v80, v208, v76
	ds_read_b64_tr_b16 v[76:77], v213 offset:18560
	ds_read_b64_tr_b16 v[78:79], v214 offset:19328
	s_waitcnt vmcnt(0)
	s_waitcnt lgkmcnt(2)
	v_mfma_f32_32x32x16_bf16 v[16:31], v[72:75], v[68:71], v[16:31]
	v_add_f32_e32 v68, v211, v80
	v_add_f32_e32 v68, v212, v68
	v_mov_b32_e32 v69, v68
	s_nop 1
	v_permlane32_swap_b32_e32 v68, v69
	v_add_f32_e32 v158, v68, v69
	v_fmac_f32_e32 v158, v159, v146
	s_waitcnt lgkmcnt(0)
	v_mfma_f32_32x32x16_bf16 v[16:31], v[76:79], v[64:67], v[16:31]
	s_barrier
	s_cbranch_scc1 .LBB0_1250
.LBB0_1238:
	s_add_i32 s98, s10, -3
	s_and_b32 s98, s98, 2
	s_mulk_i32 s98, 0x6000
	v_add_u32_e32 v144, s98, v147
	ds_read_b128 v[64:67], v144
	ds_read_b128 v[68:71], v144 offset:12288
	v_add_u32_e32 v146, s98, v148
	v_add_u32_e32 v159, s98, v149
	v_add_u32_e32 v168, s98, v150
	ds_read_b128 v[160:163], v146
	ds_read_b128 v[164:167], v146 offset:12288
	ds_read_b128 v[176:179], v159
	ds_read_b128 v[204:207], v159 offset:12288
	ds_read_b128 v[208:211], v168
	ds_read_b128 v[212:215], v168 offset:12288
	s_add_i32 s13, s10, -1
	s_cmp_ge_u32 s13, s9
	s_cbranch_scc1 .LBB0_1240
	s_and_b32 s14, s13, 2
	s_mulk_i32 s14, 0x6000
	s_add_i32 s14, s88, s14
	s_mov_b32 m0, s14
	v_lshl_add_u64 v[240:241], v[174:175], 0, v[180:181]
	global_load_lds_dwordx4 v[174:175], off
	s_add_i32 m0, s14, 0x2000
	v_mov_b32_e32 v185, v181
	global_load_lds_dwordx4 v[172:173], off
	s_add_i32 m0, s14, 0x4000
	v_lshl_add_u64 v[242:243], v[172:173], 0, v[184:185]
	v_mov_b32_e32 v187, v181
	global_load_lds_dwordx4 v[188:189], off
	v_lshl_add_u64 v[244:245], v[188:189], 0, v[186:187]
	v_lshl_add_u64 v[174:175], v[240:241], 0, v[180:181]
	v_lshl_add_u64 v[172:173], v[242:243], 0, v[184:185]
	v_lshl_add_u64 v[188:189], v[244:245], 0, v[186:187]
	s_cmp_lg_u32 s101, 0
	s_cbranch_scc1 .LBB0_1240
	s_and_b32 s14, s10, 3
	s_mulk_i32 s14, 0x6000
	s_add_i32 s14, s88, s14
	s_mov_b32 m0, s14
	s_nop 0
	global_load_lds_dwordx4 v[240:241], off
	s_add_i32 m0, s14, 0x2000
	s_nop 0
	global_load_lds_dwordx4 v[242:243], off
	s_add_i32 m0, s14, 0x4000
	s_nop 0
	global_load_lds_dwordx4 v[244:245], off

.LBB0_1242:
	s_and_b32 s14, s14, 2
	s_mulk_i32 s14, 0x6000
	s_waitcnt lgkmcnt(6)
	v_mfma_f32_32x32x16_bf16 v[80:95], v[64:67], v[112:115], 0
	v_mfma_f32_32x32x16_bf16 v[64:79], v[68:71], v[112:115], 0
	s_waitcnt lgkmcnt(4)
	v_mfma_f32_32x32x16_bf16 v[80:95], v[160:163], v[116:119], v[80:95]
	ds_read_b128 v[160:163], v144 offset:128
	ds_read_b128 v[216:219], v144 offset:12416
	v_mfma_f32_32x32x16_bf16 v[64:79], v[164:167], v[116:119], v[64:79]
	s_waitcnt lgkmcnt(4)
	v_mfma_f32_32x32x16_bf16 v[80:95], v[176:179], v[120:123], v[80:95]
	ds_read_b128 v[164:167], v146 offset:128
	ds_read_b128 v[176:179], v146 offset:12416
	v_mfma_f32_32x32x16_bf16 v[64:79], v[204:207], v[120:123], v[64:79]
	s_waitcnt lgkmcnt(4)
	v_mfma_f32_32x32x16_bf16 v[80:95], v[208:211], v[124:127], v[80:95]
	ds_read_b128 v[204:207], v159 offset:128
	ds_read_b128 v[208:211], v159 offset:12416
	v_mfma_f32_32x32x16_bf16 v[64:79], v[212:215], v[124:127], v[64:79]
	s_waitcnt lgkmcnt(4)
	v_mfma_f32_32x32x16_bf16 v[80:95], v[160:163], v[96:99], v[80:95]
	ds_read_b128 v[160:163], v168 offset:128
	ds_read_b128 v[212:215], v168 offset:12416
	v_mfma_f32_32x32x16_bf16 v[64:79], v[216:219], v[96:99], v[64:79]
	s_waitcnt lgkmcnt(4)
	v_mfma_f32_32x32x16_bf16 v[80:95], v[164:167], v[100:103], v[80:95]
	ds_read_b128 v[164:167], v144 offset:256
	ds_read_b128 v[216:219], v144 offset:12544
	v_mfma_f32_32x32x16_bf16 v[64:79], v[176:179], v[100:103], v[64:79]
	s_waitcnt lgkmcnt(4)
	v_mfma_f32_32x32x16_bf16 v[80:95], v[204:207], v[104:107], v[80:95]
	ds_read_b128 v[176:179], v146 offset:256
	ds_read_b128 v[204:207], v146 offset:12544
	v_mfma_f32_32x32x16_bf16 v[64:79], v[208:211], v[104:107], v[64:79]
	s_waitcnt lgkmcnt(4)
	v_mfma_f32_32x32x16_bf16 v[80:95], v[160:163], v[108:111], v[80:95]
	ds_read_b128 v[160:163], v159 offset:256
	ds_read_b128 v[208:211], v159 offset:12544
	v_mfma_f32_32x32x16_bf16 v[64:79], v[212:215], v[108:111], v[64:79]
	s_waitcnt lgkmcnt(4)
	v_mfma_f32_32x32x16_bf16 v[80:95], v[164:167], v[128:131], v[80:95]
	ds_read_b128 v[164:167], v168 offset:256
	ds_read_b128 v[212:215], v168 offset:12544
	v_mfma_f32_32x32x16_bf16 v[64:79], v[216:219], v[128:131], v[64:79]
	s_waitcnt lgkmcnt(4)
	v_mfma_f32_32x32x16_bf16 v[80:95], v[176:179], v[132:135], v[80:95]
	v_mfma_f32_32x32x16_bf16 v[64:79], v[204:207], v[132:135], v[64:79]
	s_waitcnt lgkmcnt(2)
	v_mfma_f32_32x32x16_bf16 v[80:95], v[160:163], v[136:139], v[80:95]
	v_mfma_f32_32x32x16_bf16 v[64:79], v[208:211], v[136:139], v[64:79]
	s_waitcnt lgkmcnt(0)
	v_mfma_f32_32x32x16_bf16 v[80:95], v[164:167], v[140:143], v[80:95]
	v_mfma_f32_32x32x16_bf16 v[64:79], v[212:215], v[140:143], v[64:79]
	s_barrier
	s_sub_i32 s15, s7, 64
	s_cmp_le_u32 s15, s44
	s_cbranch_scc1 .LBB0_1244
	v_add_u32_e32 v144, 123, v156
	v_cmp_le_i32_e64 s[16:17], 0, v144
	v_cmp_le_i32_e64 s[18:19], 32, v144
	v_cmp_le_i32_e64 vcc, 1, v144
	s_nop 4
	v_cndmask_b32_e64 v80, v199, v80, s[16:17]
	v_cmp_le_i32_e64 s[16:17], 33, v144
	v_cndmask_b32_e64 v64, v199, v64, s[18:19]
	v_cmp_le_i32_e64 s[18:19], 2, v144
	v_cndmask_b32_e64 v81, v199, v81, vcc
	v_cmp_le_i32_e64 vcc, 34, v144
	v_cndmask_b32_e64 v65, v199, v65, s[16:17]
	v_cmp_le_i32_e64 s[16:17], 3, v144
	v_cndmask_b32_e64 v82, v199, v82, s[18:19]
	v_cmp_le_i32_e64 s[18:19], 35, v144
	v_cndmask_b32_e64 v66, v199, v66, vcc
	v_cmp_le_i32_e64 vcc, 8, v144
	v_cndmask_b32_e64 v83, v199, v83, s[16:17]
	v_cmp_le_i32_e64 s[16:17], 40, v144
	v_cndmask_b32_e64 v67, v199, v67, s[18:19]
	v_cmp_le_i32_e64 s[18:19], 9, v144
	v_cndmask_b32_e64 v84, v199, v84, vcc
	v_cmp_le_i32_e64 vcc, 41, v144
	v_cndmask_b32_e64 v68, v199, v68, s[16:17]
	v_cmp_le_i32_e64 s[16:17], 10, v144
	v_cndmask_b32_e64 v85, v199, v85, s[18:19]
	v_cmp_le_i32_e64 s[18:19], 42, v144
	v_cndmask_b32_e64 v69, v199, v69, vcc
	v_cmp_le_i32_e64 vcc, 11, v144
	v_cndmask_b32_e64 v86, v199, v86, s[16:17]
	v_cmp_le_i32_e64 s[16:17], 43, v144
	v_cndmask_b32_e64 v70, v199, v70, s[18:19]
	v_cmp_le_i32_e64 s[18:19], 16, v144
	v_cndmask_b32_e64 v87, v199, v87, vcc
	v_cmp_le_i32_e64 vcc, 48, v144
	v_cndmask_b32_e64 v71, v199, v71, s[16:17]
	v_cmp_le_i32_e64 s[16:17], 17, v144
	v_cndmask_b32_e64 v88, v199, v88, s[18:19]
	v_cmp_le_i32_e64 s[18:19], 49, v144
	v_cndmask_b32_e64 v72, v199, v72, vcc
	v_cmp_le_i32_e64 vcc, 18, v144
	v_cndmask_b32_e64 v89, v199, v89, s[16:17]
	v_cmp_le_i32_e64 s[16:17], 50, v144
	v_cndmask_b32_e64 v73, v199, v73, s[18:19]
	v_cmp_le_i32_e64 s[18:19], 19, v144
	v_cndmask_b32_e64 v90, v199, v90, vcc
	v_cmp_le_i32_e64 vcc, 51, v144
	v_cndmask_b32_e64 v74, v199, v74, s[16:17]
	v_cmp_le_i32_e64 s[16:17], 24, v144
	v_cndmask_b32_e64 v91, v199, v91, s[18:19]
	v_cmp_le_i32_e64 s[18:19], 56, v144
	v_cndmask_b32_e64 v75, v199, v75, vcc
	v_cmp_le_i32_e64 vcc, 25, v144
	v_cndmask_b32_e64 v92, v199, v92, s[16:17]
	v_cmp_le_i32_e64 s[16:17], 57, v144
	v_cndmask_b32_e64 v76, v199, v76, s[18:19]
	v_cmp_le_i32_e64 s[18:19], 26, v144
	v_cndmask_b32_e64 v93, v199, v93, vcc
	v_cmp_le_i32_e64 vcc, 58, v144
	v_cndmask_b32_e64 v77, v199, v77, s[16:17]
	v_cmp_le_i32_e64 s[16:17], 27, v144
	v_cndmask_b32_e64 v94, v199, v94, s[18:19]
	v_cmp_le_i32_e64 s[18:19], 59, v144
	v_cndmask_b32_e64 v78, v199, v78, vcc
	v_cndmask_b32_e64 v95, v199, v95, s[16:17]
	v_cndmask_b32_e64 v79, v199, v79, s[18:19]

.Lf_a:
	s_cmp_ge_u32 s13, s9
	s_cbranch_scc1 .Lno_bload
	s_and_b32 s15, s10, 3
	s_mulk_i32 s15, 0x6000
	s_add_i32 s15, s88, s15
	s_mov_b32 m0, s15
	s_nop 0
	global_load_lds_dwordx4 v[240:241], off
	s_add_i32 m0, s15, 0x2000
	s_nop 0
	global_load_lds_dwordx4 v[242:243], off
	s_add_i32 m0, s15, 0x4000
	s_nop 0
	global_load_lds_dwordx4 v[244:245], off
.Lno_bload:
	v_add_u32_e32 v248, s14, v151
	v_add_u32_e32 v249, s14, v152
	ds_read_b64_tr_b16 v[224:225], v248
	ds_read_b64_tr_b16 v[226:227], v249 offset:768
	ds_read_b64_tr_b16 v[228:229], v248 offset:6144
	ds_read_b64_tr_b16 v[230:231], v249 offset:6912
	ds_read_b64_tr_b16 v[232:233], v248 offset:12288
	ds_read_b64_tr_b16 v[234:235], v249 offset:13056
	ds_read_b64_tr_b16 v[236:237], v248 offset:18432
	ds_read_b64_tr_b16 v[238:239], v249 offset:19200
	v_exp_f32_e32 v80, v80
	v_exp_f32_e32 v81, v81
	v_exp_f32_e32 v82, v82
	v_exp_f32_e32 v83, v83
	v_add_f32_e32 v146, 0, v80
	v_exp_f32_e32 v84, v84
	v_add_f32_e32 v146, v81, v146
	v_exp_f32_e32 v85, v85
	v_add_f32_e32 v146, v82, v146
	v_exp_f32_e32 v86, v86
	v_add_f32_e32 v146, v83, v146
	v_exp_f32_e32 v87, v87
	v_add_f32_e32 v146, v84, v146
	v_exp_f32_e32 v88, v88
	v_add_f32_e32 v146, v85, v146
	v_exp_f32_e32 v89, v89
	v_add_f32_e32 v146, v86, v146
	v_exp_f32_e32 v90, v90
	v_add_f32_e32 v146, v87, v146
	v_exp_f32_e32 v91, v91
	v_add_f32_e32 v146, v88, v146
	v_exp_f32_e32 v92, v92
	v_add_f32_e32 v146, v89, v146
	v_exp_f32_e32 v93, v93
	v_add_f32_e32 v146, v90, v146
	v_exp_f32_e32 v94, v94
	v_add_f32_e32 v146, v91, v146
	v_exp_f32_e32 v95, v95
	v_add_f32_e32 v146, v92, v146
	v_exp_f32_e32 v64, v64
	v_add_f32_e32 v146, v93, v146
	v_exp_f32_e32 v65, v65
	v_add_f32_e32 v146, v94, v146
	v_exp_f32_e32 v66, v66
	v_add_f32_e32 v146, v95, v146
	v_exp_f32_e32 v67, v67
	v_add_f32_e32 v146, v64, v146
	v_exp_f32_e32 v68, v68
	v_add_f32_e32 v146, v65, v146
	v_exp_f32_e32 v69, v69
	v_add_f32_e32 v146, v66, v146
	v_exp_f32_e32 v70, v70
	v_add_f32_e32 v146, v67, v146
	v_exp_f32_e32 v71, v71
	v_add_f32_e32 v146, v68, v146
	v_exp_f32_e32 v161, v72
	v_add_f32_e32 v146, v69, v146
	v_add_f32_e32 v146, v70, v146
	v_add_f32_e32 v146, v71, v146
	v_add_f32_e32 v72, v161, v146
	v_exp_f32_e32 v146, v73
	v_exp_f32_e32 v162, v74
	v_exp_f32_e32 v163, v75
	v_exp_f32_e32 v164, v76
	v_add_f32_e32 v72, v146, v72
	v_exp_f32_e32 v165, v77
	v_add_f32_e32 v72, v162, v72
	v_exp_f32_e32 v166, v78
	v_add_f32_e32 v72, v163, v72
	v_exp_f32_e32 v167, v79
	v_add_f32_e32 v72, v164, v72
	v_add_f32_e32 v72, v165, v72
	v_add_f32_e32 v72, v166, v72
	v_cvt_pk_bf16_f32 v76, v80, v81
	v_cvt_pk_bf16_f32 v77, v84, v85
	v_cvt_pk_bf16_f32 v78, v82, v83
	v_cvt_pk_bf16_f32 v79, v86, v87
	v_cvt_pk_bf16_f32 v64, v64, v65
	v_cvt_pk_bf16_f32 v65, v68, v69
	v_cvt_pk_bf16_f32 v68, v161, v146
	v_add_u32_e32 v146, s14, v151
	v_add_f32_e32 v159, v167, v72
	v_cvt_pk_bf16_f32 v72, v88, v89
	v_cvt_pk_bf16_f32 v73, v92, v93
	v_cvt_pk_bf16_f32 v74, v90, v91
	v_cvt_pk_bf16_f32 v75, v94, v95
	v_add_u32_e32 v161, s14, v152
	s_barrier
	s_waitcnt lgkmcnt(6)
	v_mfma_f32_32x32x16_bf16 v[48:63], v[224:227], v[76:79], v[48:63]
	v_cvt_pk_bf16_f32 v66, v66, v67
	v_cvt_pk_bf16_f32 v67, v70, v71
	v_cvt_pk_bf16_f32 v71, v166, v167
	v_add_u32_e32 v166, s14, v153
	v_cvt_pk_bf16_f32 v69, v164, v165
	v_cvt_pk_bf16_f32 v70, v162, v163
	v_add_u32_e32 v167, s14, v154
	ds_read_b64_tr_b16 v[162:163], v166
	ds_read_b64_tr_b16 v[164:165], v167 offset:768
	ds_read_b64_tr_b16 v[176:177], v166 offset:6144
	ds_read_b64_tr_b16 v[178:179], v167 offset:6912
	ds_read_b64_tr_b16 v[204:205], v166 offset:12288
	ds_read_b64_tr_b16 v[206:207], v167 offset:13056
	ds_read_b64_tr_b16 v[208:209], v166 offset:18432
	ds_read_b64_tr_b16 v[210:211], v167 offset:19200
	s_waitcnt lgkmcnt(12)
	v_mfma_f32_32x32x16_bf16 v[48:63], v[228:231], v[72:75], v[48:63]
	s_add_i32 s14, s10, -2
	s_and_b32 s14, s14, 3
	s_mulk_i32 s14, 0x6000
	s_waitcnt lgkmcnt(6)
	v_mfma_f32_32x32x16_bf16 v[32:47], v[162:165], v[76:79], v[32:47]
	v_mfma_f32_32x32x16_bf16 v[48:63], v[232:235], v[64:67], v[48:63]
	s_waitcnt lgkmcnt(4)
	v_mfma_f32_32x32x16_bf16 v[32:47], v[176:179], v[72:75], v[32:47]
	v_mfma_f32_32x32x16_bf16 v[48:63], v[236:239], v[68:71], v[48:63]
	ds_read_b64_tr_b16 v[80:81], v146 offset:128
	ds_read_b64_tr_b16 v[82:83], v161 offset:896
	ds_read_b64_tr_b16 v[92:93], v146 offset:6272
	ds_read_b64_tr_b16 v[94:95], v161 offset:7040
	ds_read_b64_tr_b16 v[212:213], v146 offset:12416
	ds_read_b64_tr_b16 v[214:215], v161 offset:13184
	ds_read_b64_tr_b16 v[88:89], v146 offset:18560
	ds_read_b64_tr_b16 v[90:91], v161 offset:19328
	v_add_u32_e32 v146, s14, v147
	v_add_u32_e32 v161, s14, v148
	s_waitcnt lgkmcnt(10)
	v_mfma_f32_32x32x16_bf16 v[32:47], v[204:207], v[64:67], v[32:47]
	ds_read_b64_tr_b16 v[84:85], v166 offset:128
	ds_read_b64_tr_b16 v[86:87], v167 offset:896
	ds_read_b64_tr_b16 v[162:163], v166 offset:6272
	ds_read_b64_tr_b16 v[164:165], v167 offset:7040
	ds_read_b64_tr_b16 v[176:177], v166 offset:12416
	ds_read_b64_tr_b16 v[178:179], v167 offset:13184
	ds_read_b64_tr_b16 v[204:205], v166 offset:18560
	ds_read_b64_tr_b16 v[206:207], v167 offset:19328
	v_add_u32_e32 v166, s14, v149
	v_add_u32_e32 v167, s14, v150
	s_waitcnt lgkmcnt(14)
	v_mfma_f32_32x32x16_bf16 v[0:15], v[80:83], v[76:79], v[0:15]
	s_waitcnt lgkmcnt(6)
	v_mfma_f32_32x32x16_bf16 v[16:31], v[84:87], v[76:79], v[16:31]
	v_mfma_f32_32x32x16_bf16 v[0:15], v[92:95], v[72:75], v[0:15]
	s_waitcnt lgkmcnt(4)
	v_mfma_f32_32x32x16_bf16 v[16:31], v[162:165], v[72:75], v[16:31]
	v_mfma_f32_32x32x16_bf16 v[0:15], v[212:215], v[64:67], v[0:15]
	s_waitcnt lgkmcnt(2)
	v_mfma_f32_32x32x16_bf16 v[16:31], v[176:179], v[64:67], v[16:31]
	v_mfma_f32_32x32x16_bf16 v[32:47], v[208:211], v[68:71], v[32:47]
	v_mfma_f32_32x32x16_bf16 v[0:15], v[88:91], v[68:71], v[0:15]
	s_waitcnt lgkmcnt(0)
	v_mfma_f32_32x32x16_bf16 v[16:31], v[204:207], v[68:71], v[16:31]
	ds_read_b128 v[64:67], v146
	ds_read_b128 v[68:71], v146 offset:12288
	ds_read_b128 v[162:165], v161
	ds_read_b128 v[176:179], v161 offset:12288
	ds_read_b128 v[204:207], v166
	ds_read_b128 v[208:211], v166 offset:12288
	ds_read_b128 v[212:215], v167
	ds_read_b128 v[216:219], v167 offset:12288
	s_waitcnt lgkmcnt(6)
	v_mfma_f32_32x32x16_bf16 v[80:95], v[64:67], v[112:115], 0
	v_mfma_f32_32x32x16_bf16 v[64:79], v[68:71], v[112:115], 0
	s_waitcnt lgkmcnt(4)
	v_mfma_f32_32x32x16_bf16 v[80:95], v[162:165], v[116:119], v[80:95]
	ds_read_b128 v[162:165], v146 offset:128
	ds_read_b128 v[220:223], v146 offset:12416
	v_mfma_f32_32x32x16_bf16 v[64:79], v[176:179], v[116:119], v[64:79]
	s_waitcnt lgkmcnt(4)
	v_mfma_f32_32x32x16_bf16 v[80:95], v[204:207], v[120:123], v[80:95]
	ds_read_b128 v[176:179], v161 offset:128
	ds_read_b128 v[204:207], v161 offset:12416
	v_mfma_f32_32x32x16_bf16 v[64:79], v[208:211], v[120:123], v[64:79]
	s_waitcnt lgkmcnt(4)
	v_mfma_f32_32x32x16_bf16 v[80:95], v[212:215], v[124:127], v[80:95]
	ds_read_b128 v[208:211], v166 offset:128
	ds_read_b128 v[212:215], v166 offset:12416
	v_mfma_f32_32x32x16_bf16 v[64:79], v[216:219], v[124:127], v[64:79]
	s_waitcnt lgkmcnt(4)
	v_mfma_f32_32x32x16_bf16 v[80:95], v[162:165], v[96:99], v[80:95]
	ds_read_b128 v[162:165], v167 offset:128
	ds_read_b128 v[216:219], v167 offset:12416
	v_mfma_f32_32x32x16_bf16 v[64:79], v[220:223], v[96:99], v[64:79]
	s_waitcnt lgkmcnt(4)
	v_mfma_f32_32x32x16_bf16 v[80:95], v[176:179], v[100:103], v[80:95]
	ds_read_b128 v[176:179], v146 offset:256
	ds_read_b128 v[220:223], v146 offset:12544
	v_mfma_f32_32x32x16_bf16 v[64:79], v[204:207], v[100:103], v[64:79]
	s_waitcnt lgkmcnt(4)
	v_mfma_f32_32x32x16_bf16 v[80:95], v[208:211], v[104:107], v[80:95]
	ds_read_b128 v[204:207], v161 offset:256
	ds_read_b128 v[208:211], v161 offset:12544
	v_mfma_f32_32x32x16_bf16 v[64:79], v[212:215], v[104:107], v[64:79]
	s_waitcnt lgkmcnt(4)
	v_mfma_f32_32x32x16_bf16 v[80:95], v[162:165], v[108:111], v[80:95]
	ds_read_b128 v[162:165], v166 offset:256
	ds_read_b128 v[212:215], v166 offset:12544
	v_mfma_f32_32x32x16_bf16 v[64:79], v[216:219], v[108:111], v[64:79]
	s_waitcnt lgkmcnt(4)
	v_mfma_f32_32x32x16_bf16 v[80:95], v[176:179], v[128:131], v[80:95]
	ds_read_b128 v[176:179], v167 offset:256
	ds_read_b128 v[216:219], v167 offset:12544
	v_mfma_f32_32x32x16_bf16 v[64:79], v[220:223], v[128:131], v[64:79]
	s_waitcnt lgkmcnt(4)
	v_mfma_f32_32x32x16_bf16 v[80:95], v[204:207], v[132:135], v[80:95]
	v_mfma_f32_32x32x16_bf16 v[64:79], v[208:211], v[132:135], v[64:79]
	s_waitcnt lgkmcnt(2)
	v_mfma_f32_32x32x16_bf16 v[80:95], v[162:165], v[136:139], v[80:95]
	v_mfma_f32_32x32x16_bf16 v[64:79], v[212:215], v[136:139], v[64:79]
	s_waitcnt lgkmcnt(0)
	v_mfma_f32_32x32x16_bf16 v[80:95], v[176:179], v[140:143], v[80:95]
	v_mfma_f32_32x32x16_bf16 v[64:79], v[216:219], v[140:143], v[64:79]
	s_barrier
	s_cmp_le_u32 s7, s44
	s_cbranch_scc1 .Lf_b
	v_add_u32_e32 v146, 59, v156
	v_cmp_le_i32_e64 s[16:17], 0, v146
	v_cmp_le_i32_e64 s[18:19], 32, v146
	v_cmp_le_i32_e64 vcc, 1, v146
	s_nop 4
	v_cndmask_b32_e64 v80, v199, v80, s[16:17]
	v_cmp_le_i32_e64 s[16:17], 33, v146
	v_cndmask_b32_e64 v64, v199, v64, s[18:19]
	v_cmp_le_i32_e64 s[18:19], 2, v146
	v_cndmask_b32_e64 v81, v199, v81, vcc
	v_cmp_le_i32_e64 vcc, 34, v146
	v_cndmask_b32_e64 v65, v199, v65, s[16:17]
	v_cmp_le_i32_e64 s[16:17], 3, v146
	v_cndmask_b32_e64 v82, v199, v82, s[18:19]
	v_cmp_le_i32_e64 s[18:19], 35, v146
	v_cndmask_b32_e64 v66, v199, v66, vcc
	v_cmp_le_i32_e64 vcc, 8, v146
	v_cndmask_b32_e64 v83, v199, v83, s[16:17]
	v_cmp_le_i32_e64 s[16:17], 40, v146
	v_cndmask_b32_e64 v67, v199, v67, s[18:19]
	v_cmp_le_i32_e64 s[18:19], 9, v146
	v_cndmask_b32_e64 v84, v199, v84, vcc
	v_cmp_le_i32_e64 vcc, 41, v146
	v_cndmask_b32_e64 v68, v199, v68, s[16:17]
	v_cmp_le_i32_e64 s[16:17], 10, v146
	v_cndmask_b32_e64 v85, v199, v85, s[18:19]
	v_cmp_le_i32_e64 s[18:19], 42, v146
	v_cndmask_b32_e64 v69, v199, v69, vcc
	v_cmp_le_i32_e64 vcc, 11, v146
	v_cndmask_b32_e64 v86, v199, v86, s[16:17]
	v_cmp_le_i32_e64 s[16:17], 43, v146
	v_cndmask_b32_e64 v70, v199, v70, s[18:19]
	v_cmp_le_i32_e64 s[18:19], 16, v146
	v_cndmask_b32_e64 v87, v199, v87, vcc
	v_cmp_le_i32_e64 vcc, 48, v146
	v_cndmask_b32_e64 v71, v199, v71, s[16:17]
	v_cmp_le_i32_e64 s[16:17], 17, v146
	v_cndmask_b32_e64 v88, v199, v88, s[18:19]
	v_cmp_le_i32_e64 s[18:19], 49, v146
	v_cndmask_b32_e64 v72, v199, v72, vcc
	v_cmp_le_i32_e64 vcc, 18, v146
	v_cndmask_b32_e64 v89, v199, v89, s[16:17]
	v_cmp_le_i32_e64 s[16:17], 50, v146
	v_cndmask_b32_e64 v73, v199, v73, s[18:19]
	v_cmp_le_i32_e64 s[18:19], 19, v146
	v_cndmask_b32_e64 v90, v199, v90, vcc
	v_cmp_le_i32_e64 vcc, 51, v146
	v_cndmask_b32_e64 v74, v199, v74, s[16:17]
	v_cmp_le_i32_e64 s[16:17], 24, v146
	v_cndmask_b32_e64 v91, v199, v91, s[18:19]
	v_cmp_le_i32_e64 s[18:19], 56, v146
	v_cndmask_b32_e64 v75, v199, v75, vcc
	v_cmp_le_i32_e64 vcc, 25, v146
	v_cndmask_b32_e64 v92, v199, v92, s[16:17]
	v_cmp_le_i32_e64 s[16:17], 57, v146
	v_cndmask_b32_e64 v76, v199, v76, s[18:19]
	v_cmp_le_i32_e64 s[18:19], 26, v146
	v_cndmask_b32_e64 v93, v199, v93, vcc
	v_cmp_le_i32_e64 vcc, 58, v146
	v_cndmask_b32_e64 v77, v199, v77, s[16:17]
	v_cmp_le_i32_e64 s[16:17], 27, v146
	v_cndmask_b32_e64 v94, v199, v94, s[18:19]
	v_cmp_le_i32_e64 s[18:19], 59, v146
	v_cndmask_b32_e64 v78, v199, v78, vcc
	v_cndmask_b32_e64 v95, v199, v95, s[16:17]
	v_cndmask_b32_e64 v79, v199, v79, s[18:19]
.Lf_b:
	v_add_u32_e32 v209, s14, v151
	v_add_u32_e32 v210, s14, v152
	v_add_u32_e32 v213, s14, v153
	v_add_u32_e32 v214, s14, v154
	ds_read_b64_tr_b16 v[224:225], v209
	ds_read_b64_tr_b16 v[226:227], v210 offset:768
	ds_read_b64_tr_b16 v[228:229], v209 offset:6144
	ds_read_b64_tr_b16 v[230:231], v210 offset:6912
	ds_read_b64_tr_b16 v[232:233], v209 offset:12288
	ds_read_b64_tr_b16 v[234:235], v210 offset:13056
	ds_read_b64_tr_b16 v[236:237], v209 offset:18432
	ds_read_b64_tr_b16 v[238:239], v210 offset:19200
	ds_read_b64_tr_b16 v[240:241], v213
	ds_read_b64_tr_b16 v[242:243], v214 offset:768
	ds_read_b64_tr_b16 v[244:245], v213 offset:6144
	ds_read_b64_tr_b16 v[246:247], v214 offset:6912
	v_exp_f32_e32 v170, v64
	v_exp_f32_e32 v171, v65
	v_exp_f32_e32 v176, v66
	v_exp_f32_e32 v177, v67
	v_exp_f32_e32 v178, v68
	v_exp_f32_e32 v179, v69
	v_exp_f32_e32 v161, v80
	v_exp_f32_e32 v185, v70
	v_exp_f32_e32 v162, v81
	v_exp_f32_e32 v187, v71
	v_exp_f32_e32 v163, v82
	v_exp_f32_e32 v203, v72
	v_exp_f32_e32 v164, v83
	v_exp_f32_e32 v204, v73
	v_exp_f32_e32 v165, v84
	v_exp_f32_e32 v205, v74
	v_exp_f32_e32 v166, v85
	v_exp_f32_e32 v206, v75
	v_exp_f32_e32 v167, v86
	v_exp_f32_e32 v207, v76
	v_exp_f32_e32 v168, v87
	v_exp_f32_e32 v208, v77
	v_exp_f32_e32 v88, v88
	v_exp_f32_e32 v89, v89
	v_exp_f32_e32 v90, v90
	v_exp_f32_e32 v91, v91
	v_cvt_pk_bf16_f32 v72, v161, v162
	v_cvt_pk_bf16_f32 v73, v165, v166
	v_cvt_pk_bf16_f32 v74, v163, v164
	v_cvt_pk_bf16_f32 v75, v167, v168
	v_exp_f32_e32 v92, v92
	v_exp_f32_e32 v93, v93
	v_exp_f32_e32 v94, v94
	v_exp_f32_e32 v95, v95
	v_exp_f32_e32 v211, v78
	v_mov_b32_e32 v80, v79
	v_cvt_pk_bf16_f32 v76, v88, v89
	v_cvt_pk_bf16_f32 v77, v92, v93
	v_cvt_pk_bf16_f32 v78, v90, v91
	v_cvt_pk_bf16_f32 v79, v94, v95
	v_cvt_pk_bf16_f32 v68, v170, v171
	v_cvt_pk_bf16_f32 v69, v178, v179
	v_cvt_pk_bf16_f32 v70, v176, v177
	v_cvt_pk_bf16_f32 v71, v185, v187
	v_exp_f32_e32 v212, v80
	v_cvt_pk_bf16_f32 v64, v203, v204
	v_cvt_pk_bf16_f32 v65, v207, v208
	v_cvt_pk_bf16_f32 v66, v205, v206
	v_cvt_pk_bf16_f32 v67, v211, v212
	v_add_f32_e32 v158, v158, v159
	s_addk_i32 s12, 0x1000
	s_add_i32 s11, s11, 4
	s_add_i32 s10, s10, 2
	s_addk_i32 s7, 0x80
	v_add_u32_e32 v155, 32, v155
	s_cmp_ge_u32 s13, s9
	v_add_u32_e32 v156, 0xffffff80, v156
	v_add_f32_e32 v84, 0, v161
	v_add_f32_e32 v84, v162, v84
	v_add_f32_e32 v84, v163, v84
	v_add_f32_e32 v84, v164, v84
	v_add_f32_e32 v144, v165, v84
	v_add_f32_e32 v80, v166, v144
	v_add_f32_e32 v80, v167, v80
	v_add_f32_e32 v80, v168, v80
	v_add_f32_e32 v80, v88, v80
	v_add_f32_e32 v88, v89, v80
	v_add_f32_e32 v84, v90, v88
	v_add_f32_e32 v84, v91, v84
	v_add_f32_e32 v84, v92, v84
	v_add_f32_e32 v84, v93, v84
	v_add_f32_e32 v88, v94, v84
	v_add_f32_e32 v80, v95, v88
	v_add_f32_e32 v80, v170, v80
	v_add_f32_e32 v80, v171, v80
	v_add_f32_e32 v80, v176, v80
	v_add_f32_e32 v88, v177, v80
	v_add_f32_e32 v248, v178, v88
	v_add_f32_e32 v249, v179, v248
	v_add_f32_e32 v252, v185, v249
	v_add_f32_e32 v253, v187, v252
	v_add_f32_e32 v84, v203, v253
	v_add_f32_e32 v254, v204, v84
	v_add_f32_e32 v255, v205, v254
	v_add_f32_e32 v248, v206, v255
	v_add_f32_e32 v249, v207, v248
	v_add_f32_e32 v80, v208, v249
	v_add_f32_e32 v252, v211, v80
	v_add_f32_e32 v253, v212, v252
	v_add_f32_e32 v158, v158, v253
	s_waitcnt vmcnt(3)
	s_barrier
	s_waitcnt lgkmcnt(10)
	v_mfma_f32_32x32x16_bf16 v[48:63], v[224:227], v[72:75], v[48:63]
	ds_read_b64_tr_b16 v[224:225], v213 offset:12288
	ds_read_b64_tr_b16 v[226:227], v214 offset:13056
	s_waitcnt lgkmcnt(10)
	v_mfma_f32_32x32x16_bf16 v[48:63], v[228:231], v[76:79], v[48:63]
	ds_read_b64_tr_b16 v[228:229], v213 offset:18432
	ds_read_b64_tr_b16 v[230:231], v214 offset:19200
	s_waitcnt lgkmcnt(10)
	v_mfma_f32_32x32x16_bf16 v[48:63], v[232:235], v[68:71], v[48:63]
	ds_read_b64_tr_b16 v[232:233], v209 offset:128
	ds_read_b64_tr_b16 v[234:235], v210 offset:896
	s_waitcnt lgkmcnt(10)
	v_mfma_f32_32x32x16_bf16 v[48:63], v[236:239], v[64:67], v[48:63]
	ds_read_b64_tr_b16 v[236:237], v209 offset:6272
	ds_read_b64_tr_b16 v[238:239], v210 offset:7040
	s_waitcnt lgkmcnt(10)
	v_mfma_f32_32x32x16_bf16 v[32:47], v[240:243], v[72:75], v[32:47]
	ds_read_b64_tr_b16 v[240:241], v209 offset:12416
	ds_read_b64_tr_b16 v[242:243], v210 offset:13184
	s_waitcnt lgkmcnt(10)
	v_mfma_f32_32x32x16_bf16 v[32:47], v[244:247], v[76:79], v[32:47]
	ds_read_b64_tr_b16 v[244:245], v209 offset:18560
	ds_read_b64_tr_b16 v[246:247], v210 offset:19328
	s_waitcnt lgkmcnt(10)
	v_mfma_f32_32x32x16_bf16 v[32:47], v[224:227], v[68:71], v[32:47]
	ds_read_b64_tr_b16 v[224:225], v213 offset:128
	ds_read_b64_tr_b16 v[226:227], v214 offset:896
	s_waitcnt lgkmcnt(10)
	v_mfma_f32_32x32x16_bf16 v[32:47], v[228:231], v[64:67], v[32:47]
	ds_read_b64_tr_b16 v[228:229], v213 offset:6272
	ds_read_b64_tr_b16 v[230:231], v214 offset:7040
	s_waitcnt lgkmcnt(10)
	v_mfma_f32_32x32x16_bf16 v[0:15], v[232:235], v[72:75], v[0:15]
	ds_read_b64_tr_b16 v[232:233], v213 offset:12416
	ds_read_b64_tr_b16 v[234:235], v214 offset:13184
	s_waitcnt lgkmcnt(10)
	v_mfma_f32_32x32x16_bf16 v[0:15], v[236:239], v[76:79], v[0:15]
	ds_read_b64_tr_b16 v[236:237], v213 offset:18560
	ds_read_b64_tr_b16 v[238:239], v214 offset:19328
	s_waitcnt lgkmcnt(10)
	v_mfma_f32_32x32x16_bf16 v[0:15], v[240:243], v[68:71], v[0:15]
	s_waitcnt lgkmcnt(8)
	v_mfma_f32_32x32x16_bf16 v[0:15], v[244:247], v[64:67], v[0:15]
	s_waitcnt lgkmcnt(6)
	v_mfma_f32_32x32x16_bf16 v[16:31], v[224:227], v[72:75], v[16:31]
	s_waitcnt lgkmcnt(4)
	v_mfma_f32_32x32x16_bf16 v[16:31], v[228:231], v[76:79], v[16:31]
	s_waitcnt lgkmcnt(2)
	v_mfma_f32_32x32x16_bf16 v[16:31], v[232:235], v[68:71], v[16:31]
	s_waitcnt lgkmcnt(0)
	v_mfma_f32_32x32x16_bf16 v[16:31], v[236:239], v[64:67], v[16:31]
	s_waitcnt vmcnt(0)
	s_barrier
	s_cbranch_scc1 .LBB0_1250
	s_branch .LBB0_1238
.LBB0_1250:
	s_cmp_eq_u32 s101, 0
	s_cbranch_scc1 .Lnostag_out
	s_cmp_ge_u32 s88, 0x1000
	s_cbranch_scc1 .Lnostag_out
	s_barrier
